# P0 expert conversion: the tile-tail block on the path that has already issued the next tile's 16 prefetch loads waits with vmcnt(N+16) so the prefetch stays in flight
# baseline (speedup 1.0000x reference)
.Lconv_tail_b:
	s_waitcnt vmcnt(27)
	v_mul_f32_e32 v106, 0x42800000, v106
	s_waitcnt vmcnt(26)
	v_mul_f32_e32 v110, 0x42800000, v110
	v_mov_b32_e32 v137, v131
	v_cvt_pk_fp8_f32 v137, v106, v110
	s_waitcnt vmcnt(25)
	v_mul_f32_e32 v98, 0x42800000, v98
	s_waitcnt vmcnt(24)
	v_mul_f32_e32 v102, 0x42800000, v102
	v_mov_b32_e32 v106, v131
	v_cvt_pk_fp8_f32 v137, v98, v102 op_sel:[0,0,1]
	v_mul_f32_e32 v98, 0x42800000, v115
	v_mul_f32_e32 v102, 0x42800000, v119
	v_cvt_pk_fp8_f32 v106, v98, v102
	v_mul_f32_e32 v98, 0x42800000, v107
	v_mul_f32_e32 v102, 0x42800000, v111
	v_mov_b32_e32 v107, v131
	v_cvt_pk_fp8_f32 v107, v98, v102
	v_mul_f32_e32 v98, 0x42800000, v99
	v_mul_f32_e32 v99, 0x42800000, v103
	v_mul_f32_e32 v102, 0x42800000, v120
	v_cvt_pk_fp8_f32 v107, v98, v99 op_sel:[0,0,1]
	v_mul_f32_e32 v99, 0x42800000, v116
	v_mov_b32_e32 v98, v131
	v_cvt_pk_fp8_f32 v98, v99, v102
	v_mul_f32_e32 v102, 0x42800000, v108
	v_mul_f32_e32 v108, 0x42800000, v112
	v_mov_b32_e32 v99, v131
	v_cvt_pk_fp8_f32 v99, v102, v108
	v_mul_f32_e32 v114, 0x42800000, v114
	v_mul_f32_e32 v118, 0x42800000, v118
	v_mov_b32_e32 v136, v131
	v_cvt_pk_fp8_f32 v136, v114, v118
	v_mul_f32_e32 v110, 0x42800000, v123
	v_mul_f32_e32 v114, 0x42800000, v127
	v_cvt_pk_fp8_f32 v106, v110, v114 op_sel:[0,0,1]
	v_mul_f32_e32 v103, 0x42800000, v124
	v_mul_f32_e32 v110, 0x42800000, v128
	v_mul_f32_e32 v100, 0x42800000, v100
	v_mul_f32_e32 v102, 0x42800000, v104
	v_cvt_pk_fp8_f32 v98, v103, v110 op_sel:[0,0,1]
	v_cvt_pk_fp8_f32 v99, v100, v102 op_sel:[0,0,1]
	v_mul_f32_e32 v100, 0x42800000, v117
	v_mul_f32_e32 v103, 0x42800000, v121
	v_mov_b32_e32 v102, v131
	v_cvt_pk_fp8_f32 v102, v100, v103
	v_mul_f32_e32 v100, 0x42800000, v109
	v_mul_f32_e32 v109, 0x42800000, v113
	v_mov_b32_e32 v103, v131
	v_cvt_pk_fp8_f32 v103, v100, v109
	v_mul_f32_e32 v100, 0x42800000, v101
	v_mul_f32_e32 v101, 0x42800000, v105
	s_waitcnt vmcnt(19)
	v_mul_f32_e32 v66, 0x42800000, v66
	v_cvt_pk_fp8_f32 v103, v100, v101 op_sel:[0,0,1]
	s_waitcnt vmcnt(18)
	v_mul_f32_e32 v70, 0x42800000, v70
	v_mov_b32_e32 v101, v131
	v_cvt_pk_fp8_f32 v101, v66, v70
	v_mul_f32_e32 v74, 0x42800000, v74
	v_mul_f32_e32 v78, 0x42800000, v78
	v_mov_b32_e32 v100, v131
	s_waitcnt vmcnt(17)
	v_mul_f32_e32 v66, 0x42800000, v90
	s_waitcnt vmcnt(16)
	v_mul_f32_e32 v70, 0x42800000, v94
	v_cvt_pk_fp8_f32 v100, v74, v78
	v_cvt_pk_fp8_f32 v101, v66, v70 op_sel:[0,0,1]
	v_mul_f32_e32 v70, 0x42800000, v75
	v_mul_f32_e32 v74, 0x42800000, v79
	v_mov_b32_e32 v66, v131
	v_cvt_pk_fp8_f32 v66, v70, v74
	v_mul_f32_e32 v70, 0x42800000, v67
	v_mul_f32_e32 v71, 0x42800000, v71
	v_mov_b32_e32 v67, v131
	v_cvt_pk_fp8_f32 v67, v70, v71
	v_mul_f32_e32 v70, 0x42800000, v91
	v_mul_f32_e32 v71, 0x42800000, v95
	v_mul_f32_e32 v74, 0x42800000, v80
	v_cvt_pk_fp8_f32 v67, v70, v71 op_sel:[0,0,1]
	v_mul_f32_e32 v71, 0x42800000, v76
	v_mov_b32_e32 v70, v131
	v_cvt_pk_fp8_f32 v70, v71, v74
	v_mul_f32_e32 v68, 0x42800000, v68
	v_mul_f32_e32 v72, 0x42800000, v72
	v_mov_b32_e32 v71, v131
	v_cvt_pk_fp8_f32 v71, v68, v72
	v_mul_f32_e32 v68, 0x42800000, v92
	v_mul_f32_e32 v72, 0x42800000, v96
	v_mul_f32_e32 v74, 0x42800000, v81
	v_cvt_pk_fp8_f32 v71, v68, v72 op_sel:[0,0,1]
	v_mul_f32_e32 v72, 0x42800000, v77
	v_mov_b32_e32 v68, v131
	v_cvt_pk_fp8_f32 v68, v72, v74
	v_mul_f32_e32 v72, 0x42800000, v69
	v_mul_f32_e32 v73, 0x42800000, v73
	v_mov_b32_e32 v69, v131
	v_mul_f32_e32 v122, 0x42800000, v122
	v_mul_f32_e32 v126, 0x42800000, v126
	v_cvt_pk_fp8_f32 v69, v72, v73
	v_cvt_pk_fp8_f32 v136, v122, v126 op_sel:[0,0,1]
	v_mul_f32_e32 v104, 0x42800000, v125
	v_mul_f32_e32 v108, 0x42800000, v129
	v_mul_f32_e32 v75, 0x42800000, v83
	v_mul_f32_e32 v78, 0x42800000, v87
	v_cvt_pk_fp8_f32 v102, v104, v108 op_sel:[0,0,1]
	v_mul_f32_e32 v82, 0x42800000, v82
	v_mul_f32_e32 v86, 0x42800000, v86
	v_cvt_pk_fp8_f32 v66, v75, v78 op_sel:[0,0,1]
	v_mul_f32_e32 v75, 0x42800000, v84
	v_mul_f32_e32 v76, 0x42800000, v88
	v_cvt_pk_fp8_f32 v100, v82, v86 op_sel:[0,0,1]
	v_cvt_pk_fp8_f32 v70, v75, v76 op_sel:[0,0,1]
	v_mul_f32_e32 v75, 0x42800000, v85
	v_mul_f32_e32 v76, 0x42800000, v89
	v_mul_f32_e32 v72, 0x42800000, v93
	v_mul_f32_e32 v73, 0x42800000, v97
	v_cvt_pk_fp8_f32 v68, v75, v76 op_sel:[0,0,1]
	v_cvt_pk_fp8_f32 v69, v72, v73 op_sel:[0,0,1]
	ds_write2_b64 v240, v[136:137], v[106:107] offset1:16
	ds_write2_b64 v240, v[98:99], v[102:103] offset0:32 offset1:48
	ds_write2_b64 v242, v[100:101], v[66:67] offset1:16
	ds_write2_b64 v242, v[70:71], v[68:69] offset0:32 offset1:48
	ds_read_b128 v[66:69], v244
	v_or_b32_e32 v70, 0xc0, v200
	v_cndmask_b32_e64 v70, v249, v70, s[6:7]
	v_or_b32_e32 v70, s8, v70
	v_mov_b32_e32 v71, v131
	v_lshlrev_b64 v[70:71], 11, v[70:71]
	v_lshl_add_u64 v[74:75], v[134:135], 0, v[70:71]
	ds_read_b128 v[70:73], v246
	s_waitcnt lgkmcnt(1)
	global_store_dwordx4 v[74:75], v[66:69], off nt
	v_readfirstlane_b32 s22, v224
	s_andn2_b64 vcc, exec, s[10:11]
	v_or_b32_e32 v66, 0xc8, v200
	v_cndmask_b32_e64 v66, v251, v66, s[6:7]
	v_or_b32_e32 v66, s8, v66
	v_mov_b32_e32 v67, v131
	v_lshlrev_b64 v[66:67], 11, v[66:67]
	v_lshl_add_u64 v[66:67], v[134:135], 0, v[66:67]
	s_waitcnt lgkmcnt(0)
	global_store_dwordx4 v[66:67], v[70:73], off nt
	ds_read_b128 v[66:69], v248
	s_mov_b64 s[18:19], s[12:13]
	v_or_b32_e32 v70, 0xd0, v200
	v_cndmask_b32_e64 v70, v253, v70, s[6:7]
	v_or_b32_e32 v70, s8, v70
	v_mov_b32_e32 v71, v131
	v_lshlrev_b64 v[70:71], 11, v[70:71]
	v_lshl_add_u64 v[74:75], v[134:135], 0, v[70:71]
	ds_read_b128 v[70:73], v250
	s_waitcnt lgkmcnt(1)
	global_store_dwordx4 v[74:75], v[66:69], off nt
	s_mov_b64 s[20:21], s[14:15]
	s_mov_b32 s27, s26
	v_or_b32_e32 v66, 0xd8, v200
	v_cndmask_b32_e64 v66, v218, v66, s[6:7]
	v_or_b32_e32 v66, s8, v66
	v_mov_b32_e32 v67, v131
	v_lshlrev_b64 v[66:67], 11, v[66:67]
	v_lshl_add_u64 v[66:67], v[134:135], 0, v[66:67]
	s_waitcnt lgkmcnt(0)
	global_store_dwordx4 v[66:67], v[70:73], off nt
	ds_read_b128 v[66:69], v252
	s_mov_b32 s30, s4
	v_or_b32_e32 v70, 0xe0, v200
	v_cndmask_b32_e64 v70, v222, v70, s[6:7]
	v_or_b32_e32 v70, s8, v70
	v_mov_b32_e32 v71, v131
	v_lshlrev_b64 v[70:71], 11, v[70:71]
	v_lshl_add_u64 v[74:75], v[134:135], 0, v[70:71]
	ds_read_b128 v[70:73], v204
	s_waitcnt lgkmcnt(1)
	global_store_dwordx4 v[74:75], v[66:69], off nt
	s_mov_b32 s29, s24
	s_mov_b32 s28, s25
	v_or_b32_e32 v66, 0xe8, v200
	v_cndmask_b32_e64 v66, v226, v66, s[6:7]
	v_or_b32_e32 v66, s8, v66
	v_mov_b32_e32 v67, v131
	v_lshlrev_b64 v[66:67], 11, v[66:67]
	v_lshl_add_u64 v[66:67], v[134:135], 0, v[66:67]
	s_waitcnt lgkmcnt(0)
	global_store_dwordx4 v[66:67], v[70:73], off nt
	ds_read_b128 v[66:69], v216
	s_nop 0
	v_or_b32_e32 v70, 0xf0, v200
	v_cndmask_b32_e64 v70, v230, v70, s[6:7]
	v_or_b32_e32 v70, s8, v70
	v_mov_b32_e32 v71, v131
	v_lshlrev_b64 v[70:71], 11, v[70:71]
	v_lshl_add_u64 v[74:75], v[134:135], 0, v[70:71]
	ds_read_b128 v[70:73], v220
	s_waitcnt lgkmcnt(1)
	global_store_dwordx4 v[74:75], v[66:69], off nt
	s_nop 1
	v_or_b32_e32 v66, 0xf8, v200
	v_cndmask_b32_e64 v66, v234, v66, s[6:7]
	v_or_b32_e32 v66, s8, v66
	v_mov_b32_e32 v67, v131
	v_lshlrev_b64 v[66:67], 11, v[66:67]
	v_lshl_add_u64 v[66:67], v[134:135], 0, v[66:67]
	s_waitcnt lgkmcnt(0)
	global_store_dwordx4 v[66:67], v[70:73], off nt
	s_cbranch_vccz .LBB0_182
	s_branch .LBB0_171
